# only P4 prefetch fix + P3 scan load batching
# speedup vs baseline: 1.0080x; 1.0080x over previous
_Z6mk_fwd4Args:
	s_mov_b32 s100, -1
	s_load_dword s84, s[0:1], 0xd0
	s_load_dwordx4 s[4:7], s[0:1], 0xc0
	s_mov_b32 s87, s2
	s_add_u32 s2, s0, 0xd0
	s_addc_u32 s3, s1, 0
	v_readfirstlane_b32 s92, v0
	s_waitcnt lgkmcnt(0)
	v_writelane_b32 v242, s4, 0
	s_mov_b32 s93, s87
	s_nop 0
	v_writelane_b32 v242, s5, 1
	v_writelane_b32 v242, s6, 2
	v_writelane_b32 v242, s7, 3
	v_writelane_b32 v242, s2, 4
	s_nop 1
	v_writelane_b32 v242, s3, 5
	s_and_b32 s3, s84, 7
	s_mov_b32 s2, 0
	s_cmp_lg_u32 s3, 0
	s_cbranch_scc1 .LBB0_2
	s_ashr_i32 s4, s87, 31
	s_lshr_b32 s4, s4, 29
	s_add_i32 s4, s87, s4
	s_and_b32 s5, s4, -8
	s_ashr_i32 s3, s84, 3
	s_sub_i32 s5, s87, s5
	s_mul_i32 s3, s3, s5
	s_ashr_i32 s4, s4, 3
	s_add_i32 s93, s3, s4

.LBB0_708:
	ds_read_b128 v[18:21], v225
	ds_read_b128 v[22:25], v225 offset:1024
	ds_read_b128 v[26:29], v225 offset:2048
	ds_read_b128 v[30:33], v225 offset:3072
	ds_read_b128 v[2:5], v226
	ds_read_b128 v[6:9], v226 offset:1024
	ds_read_b128 v[10:13], v226 offset:2048
	ds_read_b128 v[14:17], v226 offset:3072
	s_cmp_eq_u32 s56, 12
	s_cselect_b64 s[36:37], -1, 0
	s_add_u32 s34, s62, s30
	s_addc_u32 s35, s63, s31
	s_add_u32 s34, s34, 0x80
	s_addc_u32 s35, s35, 0
	s_add_i32 m0, s43, 0xc000
	s_add_i32 s57, s43, 0xe000
	s_cmp_lg_u32 s56, 12
	ds_read_b128 v[58:61], v227
	ds_read_b128 v[62:65], v227 offset:1024
	ds_read_b128 v[50:53], v227 offset:2048
	ds_read_b128 v[54:57], v227 offset:3072
	ds_read_b128 v[42:45], v227 offset:4096
	ds_read_b128 v[46:49], v227 offset:5120
	ds_read_b128 v[34:37], v227 offset:6144
	ds_read_b128 v[38:41], v227 offset:7168
	s_nop 0
	global_load_lds_dwordx4 v198, s[34:35]
	s_mov_b32 m0, s57
	s_nop 0
	global_load_lds_dwordx4 v202, s[34:35]
	s_cbranch_scc1 .LBB0_710
	v_mov_b64_e32 v[216:217], v[212:213]
	v_mov_b64_e32 v[218:219], v[210:211]
	v_mov_b32_e32 v202, v212
	v_mov_b32_e32 v198, v210
	v_mov_b32_e32 v204, v195
	v_mov_b32_e32 v200, v1
	s_branch .LBB0_711

.LBB0_713:
	s_and_b64 vcc, exec, s[74:75]
	s_cbranch_vccz .LBB0_715
	s_barrier
.LBB0_715:
	s_ashr_i32 s29, s28, 31
	s_lshl_b64 s[34:35], s[28:29], 14
	v_readlane_b32 s16, v242, 6
	v_lshl_or_b32 v18, s3, 7, v224
	v_readlane_b32 s28, v242, 18
	v_readlane_b32 s30, v242, 20
	v_readlane_b32 s29, v242, 19
	v_readlane_b32 s31, v242, 21
	s_add_u32 s28, s30, s34
	v_lshlrev_b32_e32 v2, 1, v18
	s_addc_u32 s29, s31, s35
	v_ashrrev_i32_e32 v3, 31, v2
	s_ashr_i32 s3, s2, 31
	v_lshl_add_u64 v[2:3], v[2:3], 2, s[28:29]
	v_lshl_add_u64 v[22:23], s[2:3], 2, v[214:215]
	global_load_dword v21, v[22:23], off
	global_load_dwordx4 v[14:17], v[2:3], off
	global_load_dwordx4 v[10:13], v[2:3], off offset:16
	global_load_dwordx4 v[6:9], v[2:3], off offset:32
	s_nop 0
	global_load_dwordx4 v[2:5], v[2:3], off offset:48
	s_nop 0
	global_load_dword v27, v[22:23], off offset:64
	global_load_dword v52, v[22:23], off offset:128
	global_load_dword v53, v[22:23], off offset:192
	global_load_dword v54, v[22:23], off offset:512
	global_load_dword v26, v[22:23], off offset:576
	global_load_dword v25, v[22:23], off offset:640
	global_load_dword v24, v[22:23], off offset:704
	v_mov_b32_e32 v29, v199
	v_mov_b32_e32 v28, v199
	s_lshl_b32 s2, s33, 8
	v_add_u32_e32 v20, s2, v201
	v_ashrrev_i32_e32 v19, 31, v18
	s_andn2_b64 vcc, exec, s[8:9]
	v_readlane_b32 s17, v242, 7
	v_readlane_b32 s18, v242, 8
	v_readlane_b32 s19, v242, 9
	v_readlane_b32 s20, v242, 10
	v_readlane_b32 s21, v242, 11
	v_readlane_b32 s22, v242, 12
	v_readlane_b32 s23, v242, 13
	v_readlane_b32 s24, v242, 14
	v_readlane_b32 s25, v242, 15
	v_readlane_b32 s26, v242, 16
	v_readlane_b32 s27, v242, 17
	s_waitcnt vmcnt(0)
	v_mul_f32_e32 v30, 0x39800000, v21
	v_mov_b32_e32 v22, v14
	v_mov_b32_e32 v23, v16
	v_mov_b32_e32 v16, v15
	v_mov_b32_e32 v14, v10
	v_mov_b32_e32 v15, v12
	v_mov_b32_e32 v12, v11
	v_mov_b32_e32 v10, v6
	v_mov_b32_e32 v11, v8
	v_pk_fma_f32 v[36:37], v[184:185], v[30:31], v[12:13] op_sel_hi:[1,0,1]
	v_pk_fma_f32 v[38:39], v[186:187], v[30:31], v[10:11] op_sel_hi:[1,0,1]
	v_pk_fma_f32 v[34:35], v[192:193], v[30:31], v[14:15] op_sel_hi:[1,0,1]
	v_med3_f32 v36, v36, s54, v228
	v_med3_f32 v37, v37, s54, v228
	v_min_f32_e32 v38, 0x40e00000, v38
	v_min_f32_e32 v39, 0x40e00000, v39
	v_min_f32_e32 v34, 0x40e00000, v34
	v_min_f32_e32 v35, 0x40e00000, v35
	v_pk_fma_f32 v[36:37], v[36:37], 4.0, 4.0 op_sel_hi:[1,0,0]
	v_pk_mul_f32 v[48:49], v[38:39], s[76:77] op_sel_hi:[1,0]
	v_mov_b32_e32 v8, v7
	v_mov_b32_e32 v6, v2
	v_mov_b32_e32 v7, v4
	v_pk_mul_f32 v[46:47], v[34:35], s[76:77] op_sel_hi:[1,0]
	v_pk_mul_f32 v[34:35], v[34:35], v[36:37]
	v_exp_f32_e32 v36, v48
	v_exp_f32_e32 v37, v49
	v_mov_b32_e32 v4, v3
	v_pk_fma_f32 v[2:3], v[190:191], v[30:31], v[22:23] op_sel_hi:[1,0,1]
	v_pk_fma_f32 v[40:41], v[178:179], v[30:31], v[8:9] op_sel_hi:[1,0,1]
	v_pk_fma_f32 v[42:43], v[188:189], v[30:31], v[6:7] op_sel_hi:[1,0,1]
	v_min_f32_e32 v2, 0x40e00000, v2
	v_min_f32_e32 v3, 0x40e00000, v3
	v_med3_f32 v40, v40, s54, v228
	v_med3_f32 v41, v41, s54, v228
	v_min_f32_e32 v42, 0x40e00000, v42
	v_min_f32_e32 v43, 0x40e00000, v43
	v_pk_fma_f32 v[32:33], v[182:183], v[30:31], v[16:17] op_sel_hi:[1,0,1]
	v_pk_mul_f32 v[44:45], v[2:3], s[76:77] op_sel_hi:[1,0]
	v_pk_fma_f32 v[40:41], v[40:41], 4.0, 4.0 op_sel_hi:[1,0,0]
	v_pk_mul_f32 v[50:51], v[42:43], s[76:77] op_sel_hi:[1,0]
	v_med3_f32 v32, v32, s54, v228
	v_med3_f32 v33, v33, s54, v228
	v_exp_f32_e32 v44, v44
	v_exp_f32_e32 v45, v45
	v_pk_mul_f32 v[38:39], v[38:39], v[40:41]
	v_exp_f32_e32 v40, v50
	v_exp_f32_e32 v41, v51
	v_pk_add_f32 v[36:37], v[36:37], 1.0 op_sel_hi:[1,0]
	v_pk_fma_f32 v[30:31], v[180:181], v[30:31], v[4:5] op_sel_hi:[1,0,1]
	v_pk_fma_f32 v[32:33], v[32:33], 4.0, 4.0 op_sel_hi:[1,0,0]
	v_rcp_f32_e32 v36, v36
	v_rcp_f32_e32 v37, v37
	v_med3_f32 v30, v30, s54, v228
	v_med3_f32 v31, v31, s54, v228
	v_pk_mul_f32 v[2:3], v[2:3], v[32:33]
	v_exp_f32_e32 v32, v46
	v_exp_f32_e32 v33, v47
	v_pk_fma_f32 v[30:31], v[30:31], 4.0, 4.0 op_sel_hi:[1,0,0]
	v_pk_add_f32 v[40:41], v[40:41], 1.0 op_sel_hi:[1,0]
	v_pk_mul_f32 v[30:31], v[42:43], v[30:31]
	v_pk_add_f32 v[42:43], v[44:45], 1.0 op_sel_hi:[1,0]
	v_rcp_f32_e32 v40, v40
	v_rcp_f32_e32 v42, v42
	v_rcp_f32_e32 v43, v43
	v_rcp_f32_e32 v41, v41
	v_pk_mul_f32 v[36:37], v[38:39], v[36:37]
	v_pk_add_f32 v[32:33], v[32:33], 1.0 op_sel_hi:[1,0]
	v_cvt_pk_fp8_f32 v29, v36, v37
	v_rcp_f32_e32 v32, v32
	v_rcp_f32_e32 v33, v33
	v_pk_mul_f32 v[2:3], v[2:3], v[42:43]
	v_pk_mul_f32 v[30:31], v[30:31], v[40:41]
	v_cvt_pk_fp8_f32 v28, v2, v3
	v_cvt_pk_fp8_f32 v29, v30, v31 op_sel:[0,0,1]
	v_mul_f32_e32 v30, 0x39800000, v27
	v_pk_mul_f32 v[2:3], v[34:35], v[32:33]
	v_pk_fma_f32 v[32:33], v[174:175], v[30:31], v[22:23] op_sel_hi:[1,0,1]
	v_cvt_pk_fp8_f32 v28, v2, v3 op_sel:[0,0,1]
	v_min_f32_e32 v32, 0x40e00000, v32
	v_min_f32_e32 v33, 0x40e00000, v33
	v_pk_mul_f32 v[34:35], v[32:33], s[76:77] op_sel_hi:[1,0]
	v_ashrrev_i32_e32 v21, 31, v20
	v_exp_f32_e32 v34, v34
	v_exp_f32_e32 v35, v35
	v_lshlrev_b64 v[2:3], 11, v[20:21]
	v_lshl_add_u64 v[2:3], s[66:67], 0, v[2:3]
	v_lshl_add_u64 v[2:3], v[2:3], 0, v[18:19]
	global_store_dwordx2 v[2:3], v[28:29], off
	v_pk_add_f32 v[28:29], v[34:35], 1.0 op_sel_hi:[1,0]
	v_pk_fma_f32 v[2:3], v[170:171], v[30:31], v[16:17] op_sel_hi:[1,0,1]
	v_rcp_f32_e32 v28, v28
	v_rcp_f32_e32 v29, v29
	v_med3_f32 v2, v2, s54, v228
	v_med3_f32 v3, v3, s54, v228
	v_pk_fma_f32 v[2:3], v[2:3], 4.0, 4.0 op_sel_hi:[1,0,0]
	v_mov_b32_e32 v38, v199
	v_pk_mul_f32 v[2:3], v[32:33], v[2:3]
	v_pk_fma_f32 v[32:33], v[172:173], v[30:31], v[12:13] op_sel_hi:[1,0,1]
	v_pk_mul_f32 v[2:3], v[2:3], v[28:29]
	v_pk_fma_f32 v[28:29], v[176:177], v[30:31], v[14:15] op_sel_hi:[1,0,1]
	v_med3_f32 v32, v32, s54, v228
	v_min_f32_e32 v28, 0x40e00000, v28
	v_min_f32_e32 v29, 0x40e00000, v29
	v_pk_mul_f32 v[34:35], v[28:29], s[76:77] op_sel_hi:[1,0]
	v_med3_f32 v33, v33, s54, v228
	v_exp_f32_e32 v34, v34
	v_exp_f32_e32 v35, v35
	v_pk_fma_f32 v[32:33], v[32:33], 4.0, 4.0 op_sel_hi:[1,0,0]
	v_cvt_pk_fp8_f32 v38, v2, v3
	v_pk_mul_f32 v[28:29], v[28:29], v[32:33]
	v_pk_fma_f32 v[32:33], v[166:167], v[30:31], v[10:11] op_sel_hi:[1,0,1]
	v_pk_add_f32 v[34:35], v[34:35], 1.0 op_sel_hi:[1,0]
	v_min_f32_e32 v32, 0x40e00000, v32
	v_min_f32_e32 v33, 0x40e00000, v33
	v_pk_mul_f32 v[36:37], v[32:33], s[76:77] op_sel_hi:[1,0]
	v_rcp_f32_e32 v34, v34
	v_rcp_f32_e32 v35, v35
	v_exp_f32_e32 v36, v36
	v_exp_f32_e32 v37, v37
	v_mov_b32_e32 v39, v199
	v_pk_mul_f32 v[28:29], v[28:29], v[34:35]
	v_pk_fma_f32 v[34:35], v[162:163], v[30:31], v[8:9] op_sel_hi:[1,0,1]
	v_pk_add_f32 v[36:37], v[36:37], 1.0 op_sel_hi:[1,0]
	v_med3_f32 v34, v34, s54, v228
	v_rcp_f32_e32 v36, v36
	v_rcp_f32_e32 v37, v37
	v_med3_f32 v35, v35, s54, v228
	v_pk_fma_f32 v[34:35], v[34:35], 4.0, 4.0 op_sel_hi:[1,0,0]
	v_cvt_pk_fp8_f32 v38, v28, v29 op_sel:[0,0,1]
	v_pk_mul_f32 v[32:33], v[32:33], v[34:35]
	v_pk_fma_f32 v[34:35], v[168:169], v[30:31], v[6:7] op_sel_hi:[1,0,1]
	v_pk_mul_f32 v[32:33], v[32:33], v[36:37]
	v_min_f32_e32 v34, 0x40e00000, v34
	v_min_f32_e32 v35, 0x40e00000, v35
	v_pk_mul_f32 v[36:37], v[34:35], s[76:77] op_sel_hi:[1,0]
	v_pk_fma_f32 v[30:31], v[164:165], v[30:31], v[4:5] op_sel_hi:[1,0,1]
	v_exp_f32_e32 v36, v36
	v_exp_f32_e32 v37, v37
	v_med3_f32 v30, v30, s54, v228
	v_med3_f32 v31, v31, s54, v228
	v_cvt_pk_fp8_f32 v39, v32, v33
	v_pk_add_f32 v[36:37], v[36:37], 1.0 op_sel_hi:[1,0]
	v_pk_fma_f32 v[30:31], v[30:31], 4.0, 4.0 op_sel_hi:[1,0,0]
	v_rcp_f32_e32 v36, v36
	v_rcp_f32_e32 v37, v37
	v_mul_f32_e32 v28, 0x39800000, v52
	v_pk_mul_f32 v[2:3], v[34:35], v[30:31]
	v_pk_fma_f32 v[30:31], v[158:159], v[28:29], v[22:23] op_sel_hi:[1,0,1]
	v_pk_mul_f32 v[2:3], v[2:3], v[36:37]
	v_min_f32_e32 v30, 0x40e00000, v30
	v_min_f32_e32 v31, 0x40e00000, v31
	v_cvt_pk_fp8_f32 v39, v2, v3 op_sel:[0,0,1]
	v_add_u32_e32 v2, s2, v220
	v_pk_mul_f32 v[32:33], v[30:31], s[76:77] op_sel_hi:[1,0]
	v_ashrrev_i32_e32 v3, 31, v2
	v_exp_f32_e32 v32, v32
	v_exp_f32_e32 v33, v33
	v_lshlrev_b64 v[2:3], 11, v[2:3]
	v_lshl_add_u64 v[2:3], s[66:67], 0, v[2:3]
	v_lshl_add_u64 v[2:3], v[2:3], 0, v[18:19]
	global_store_dwordx2 v[2:3], v[38:39], off
	v_pk_fma_f32 v[2:3], v[154:155], v[28:29], v[16:17] op_sel_hi:[1,0,1]
	v_pk_add_f32 v[32:33], v[32:33], 1.0 op_sel_hi:[1,0]
	v_med3_f32 v2, v2, s54, v228
	v_rcp_f32_e32 v32, v32
	v_rcp_f32_e32 v33, v33
	v_med3_f32 v3, v3, s54, v228
	v_pk_fma_f32 v[2:3], v[2:3], 4.0, 4.0 op_sel_hi:[1,0,0]
	v_mov_b32_e32 v38, v199
	v_pk_mul_f32 v[2:3], v[30:31], v[2:3]
	v_pk_fma_f32 v[30:31], v[160:161], v[28:29], v[14:15] op_sel_hi:[1,0,1]
	v_pk_mul_f32 v[2:3], v[2:3], v[32:33]
	v_min_f32_e32 v30, 0x40e00000, v30
	v_min_f32_e32 v31, 0x40e00000, v31
	v_pk_fma_f32 v[32:33], v[156:157], v[28:29], v[12:13] op_sel_hi:[1,0,1]
	v_pk_mul_f32 v[34:35], v[30:31], s[76:77] op_sel_hi:[1,0]
	v_med3_f32 v32, v32, s54, v228
	v_exp_f32_e32 v34, v34
	v_exp_f32_e32 v35, v35
	v_med3_f32 v33, v33, s54, v228
	v_pk_fma_f32 v[32:33], v[32:33], 4.0, 4.0 op_sel_hi:[1,0,0]
	v_cvt_pk_fp8_f32 v38, v2, v3
	v_pk_mul_f32 v[30:31], v[30:31], v[32:33]
	v_pk_fma_f32 v[32:33], v[150:151], v[28:29], v[10:11] op_sel_hi:[1,0,1]
	v_pk_add_f32 v[34:35], v[34:35], 1.0 op_sel_hi:[1,0]
	v_min_f32_e32 v32, 0x40e00000, v32
	v_min_f32_e32 v33, 0x40e00000, v33
	v_pk_mul_f32 v[36:37], v[32:33], s[76:77] op_sel_hi:[1,0]
	v_rcp_f32_e32 v34, v34
	v_rcp_f32_e32 v35, v35
	v_exp_f32_e32 v36, v36
	v_exp_f32_e32 v37, v37
	v_mov_b32_e32 v39, v199
	v_pk_mul_f32 v[30:31], v[30:31], v[34:35]
	v_pk_fma_f32 v[34:35], v[146:147], v[28:29], v[8:9] op_sel_hi:[1,0,1]
	v_pk_add_f32 v[36:37], v[36:37], 1.0 op_sel_hi:[1,0]
	v_med3_f32 v34, v34, s54, v228
	v_rcp_f32_e32 v36, v36
	v_rcp_f32_e32 v37, v37
	v_med3_f32 v35, v35, s54, v228
	v_pk_fma_f32 v[34:35], v[34:35], 4.0, 4.0 op_sel_hi:[1,0,0]
	v_cvt_pk_fp8_f32 v38, v30, v31 op_sel:[0,0,1]
	v_pk_mul_f32 v[32:33], v[32:33], v[34:35]
	v_pk_fma_f32 v[34:35], v[152:153], v[28:29], v[6:7] op_sel_hi:[1,0,1]
	v_pk_mul_f32 v[32:33], v[32:33], v[36:37]
	v_min_f32_e32 v34, 0x40e00000, v34
	v_min_f32_e32 v35, 0x40e00000, v35
	v_pk_mul_f32 v[36:37], v[34:35], s[76:77] op_sel_hi:[1,0]
	v_pk_fma_f32 v[28:29], v[148:149], v[28:29], v[4:5] op_sel_hi:[1,0,1]
	v_exp_f32_e32 v36, v36
	v_exp_f32_e32 v37, v37
	v_med3_f32 v28, v28, s54, v228
	v_med3_f32 v29, v29, s54, v228
	v_pk_fma_f32 v[28:29], v[28:29], 4.0, 4.0 op_sel_hi:[1,0,0]
	v_pk_add_f32 v[36:37], v[36:37], 1.0 op_sel_hi:[1,0]
	v_cvt_pk_fp8_f32 v39, v32, v33
	v_rcp_f32_e32 v36, v36
	v_rcp_f32_e32 v37, v37
	v_pk_mul_f32 v[2:3], v[34:35], v[28:29]
	v_mul_f32_e32 v28, 0x39800000, v53
	v_pk_fma_f32 v[30:31], v[142:143], v[28:29], v[22:23] op_sel_hi:[1,0,1]
	v_pk_mul_f32 v[2:3], v[2:3], v[36:37]
	v_min_f32_e32 v30, 0x40e00000, v30
	v_min_f32_e32 v31, 0x40e00000, v31
	v_cvt_pk_fp8_f32 v39, v2, v3 op_sel:[0,0,1]
	v_add_u32_e32 v2, s2, v221
	v_pk_mul_f32 v[32:33], v[30:31], s[76:77] op_sel_hi:[1,0]
	v_ashrrev_i32_e32 v3, 31, v2
	v_exp_f32_e32 v32, v32
	v_exp_f32_e32 v33, v33
	v_lshlrev_b64 v[2:3], 11, v[2:3]
	v_lshl_add_u64 v[2:3], s[66:67], 0, v[2:3]
	v_lshl_add_u64 v[2:3], v[2:3], 0, v[18:19]
	global_store_dwordx2 v[2:3], v[38:39], off
	v_pk_fma_f32 v[2:3], v[138:139], v[28:29], v[16:17] op_sel_hi:[1,0,1]
	v_pk_add_f32 v[32:33], v[32:33], 1.0 op_sel_hi:[1,0]
	v_med3_f32 v2, v2, s54, v228
	v_rcp_f32_e32 v32, v32
	v_rcp_f32_e32 v33, v33
	v_med3_f32 v3, v3, s54, v228
	v_pk_fma_f32 v[2:3], v[2:3], 4.0, 4.0 op_sel_hi:[1,0,0]
	v_mov_b32_e32 v38, v199
	v_pk_mul_f32 v[2:3], v[30:31], v[2:3]
	v_pk_fma_f32 v[30:31], v[144:145], v[28:29], v[14:15] op_sel_hi:[1,0,1]
	v_pk_mul_f32 v[2:3], v[2:3], v[32:33]
	v_min_f32_e32 v30, 0x40e00000, v30
	v_min_f32_e32 v31, 0x40e00000, v31
	v_pk_fma_f32 v[32:33], v[140:141], v[28:29], v[12:13] op_sel_hi:[1,0,1]
	v_pk_mul_f32 v[34:35], v[30:31], s[76:77] op_sel_hi:[1,0]
	v_med3_f32 v32, v32, s54, v228
	v_exp_f32_e32 v34, v34
	v_exp_f32_e32 v35, v35
	v_med3_f32 v33, v33, s54, v228
	v_pk_fma_f32 v[32:33], v[32:33], 4.0, 4.0 op_sel_hi:[1,0,0]
	v_cvt_pk_fp8_f32 v38, v2, v3
	v_pk_mul_f32 v[30:31], v[30:31], v[32:33]
	v_pk_fma_f32 v[32:33], v[134:135], v[28:29], v[10:11] op_sel_hi:[1,0,1]
	v_pk_add_f32 v[34:35], v[34:35], 1.0 op_sel_hi:[1,0]
	v_min_f32_e32 v32, 0x40e00000, v32
	v_min_f32_e32 v33, 0x40e00000, v33
	v_pk_mul_f32 v[36:37], v[32:33], s[76:77] op_sel_hi:[1,0]
	v_rcp_f32_e32 v34, v34
	v_rcp_f32_e32 v35, v35
	v_exp_f32_e32 v36, v36
	v_exp_f32_e32 v37, v37
	v_mov_b32_e32 v39, v199
	v_pk_mul_f32 v[30:31], v[30:31], v[34:35]
	v_pk_fma_f32 v[34:35], v[130:131], v[28:29], v[8:9] op_sel_hi:[1,0,1]
	v_pk_add_f32 v[36:37], v[36:37], 1.0 op_sel_hi:[1,0]
	v_med3_f32 v34, v34, s54, v228
	v_rcp_f32_e32 v36, v36
	v_rcp_f32_e32 v37, v37
	v_med3_f32 v35, v35, s54, v228
	v_pk_fma_f32 v[34:35], v[34:35], 4.0, 4.0 op_sel_hi:[1,0,0]
	v_cvt_pk_fp8_f32 v38, v30, v31 op_sel:[0,0,1]
	v_pk_mul_f32 v[32:33], v[32:33], v[34:35]
	v_pk_fma_f32 v[34:35], v[136:137], v[28:29], v[6:7] op_sel_hi:[1,0,1]
	v_pk_mul_f32 v[32:33], v[32:33], v[36:37]
	v_min_f32_e32 v34, 0x40e00000, v34
	v_min_f32_e32 v35, 0x40e00000, v35
	v_pk_mul_f32 v[36:37], v[34:35], s[76:77] op_sel_hi:[1,0]
	v_pk_fma_f32 v[28:29], v[132:133], v[28:29], v[4:5] op_sel_hi:[1,0,1]
	v_exp_f32_e32 v36, v36
	v_exp_f32_e32 v37, v37
	v_med3_f32 v28, v28, s54, v228
	v_med3_f32 v29, v29, s54, v228
	v_pk_fma_f32 v[28:29], v[28:29], 4.0, 4.0 op_sel_hi:[1,0,0]
	v_pk_add_f32 v[36:37], v[36:37], 1.0 op_sel_hi:[1,0]
	v_cvt_pk_fp8_f32 v39, v32, v33
	v_rcp_f32_e32 v36, v36
	v_rcp_f32_e32 v37, v37
	v_pk_mul_f32 v[2:3], v[34:35], v[28:29]
	v_mul_f32_e32 v28, 0x39800000, v54
	v_pk_fma_f32 v[30:31], v[126:127], v[28:29], v[22:23] op_sel_hi:[1,0,1]
	v_pk_mul_f32 v[2:3], v[2:3], v[36:37]
	v_min_f32_e32 v30, 0x40e00000, v30
	v_min_f32_e32 v31, 0x40e00000, v31
	v_cvt_pk_fp8_f32 v39, v2, v3 op_sel:[0,0,1]
	v_add_u32_e32 v2, s2, v223
	v_pk_mul_f32 v[32:33], v[30:31], s[76:77] op_sel_hi:[1,0]
	v_ashrrev_i32_e32 v3, 31, v2
	v_exp_f32_e32 v32, v32
	v_exp_f32_e32 v33, v33
	v_lshlrev_b64 v[2:3], 11, v[2:3]
	v_lshl_add_u64 v[2:3], s[66:67], 0, v[2:3]
	v_lshl_add_u64 v[2:3], v[2:3], 0, v[18:19]
	global_store_dwordx2 v[2:3], v[38:39], off
	v_pk_fma_f32 v[2:3], v[122:123], v[28:29], v[16:17] op_sel_hi:[1,0,1]
	v_pk_add_f32 v[32:33], v[32:33], 1.0 op_sel_hi:[1,0]
	v_med3_f32 v2, v2, s54, v228
	v_rcp_f32_e32 v32, v32
	v_rcp_f32_e32 v33, v33
	v_med3_f32 v3, v3, s54, v228
	v_pk_fma_f32 v[2:3], v[2:3], 4.0, 4.0 op_sel_hi:[1,0,0]
	v_mov_b32_e32 v38, v199
	v_pk_mul_f32 v[2:3], v[30:31], v[2:3]
	v_pk_fma_f32 v[30:31], v[128:129], v[28:29], v[14:15] op_sel_hi:[1,0,1]
	v_pk_mul_f32 v[2:3], v[2:3], v[32:33]
	v_min_f32_e32 v30, 0x40e00000, v30
	v_min_f32_e32 v31, 0x40e00000, v31
	v_pk_fma_f32 v[32:33], v[124:125], v[28:29], v[12:13] op_sel_hi:[1,0,1]
	v_pk_mul_f32 v[34:35], v[30:31], s[76:77] op_sel_hi:[1,0]
	v_med3_f32 v32, v32, s54, v228
	v_exp_f32_e32 v34, v34
	v_exp_f32_e32 v35, v35
	v_med3_f32 v33, v33, s54, v228
	v_pk_fma_f32 v[32:33], v[32:33], 4.0, 4.0 op_sel_hi:[1,0,0]
	v_mov_b32_e32 v39, v199
	v_pk_mul_f32 v[30:31], v[30:31], v[32:33]
	v_pk_fma_f32 v[32:33], v[118:119], v[28:29], v[10:11] op_sel_hi:[1,0,1]
	v_pk_add_f32 v[34:35], v[34:35], 1.0 op_sel_hi:[1,0]
	v_min_f32_e32 v32, 0x40e00000, v32
	v_min_f32_e32 v33, 0x40e00000, v33
	v_pk_mul_f32 v[36:37], v[32:33], s[76:77] op_sel_hi:[1,0]
	v_rcp_f32_e32 v34, v34
	v_rcp_f32_e32 v35, v35
	v_exp_f32_e32 v36, v36
	v_exp_f32_e32 v37, v37
	v_cvt_pk_fp8_f32 v38, v2, v3
	v_pk_mul_f32 v[30:31], v[30:31], v[34:35]
	v_pk_fma_f32 v[34:35], v[114:115], v[28:29], v[8:9] op_sel_hi:[1,0,1]
	v_pk_add_f32 v[36:37], v[36:37], 1.0 op_sel_hi:[1,0]
	v_med3_f32 v34, v34, s54, v228
	v_rcp_f32_e32 v36, v36
	v_rcp_f32_e32 v37, v37
	v_med3_f32 v35, v35, s54, v228
	v_pk_fma_f32 v[34:35], v[34:35], 4.0, 4.0 op_sel_hi:[1,0,0]
	v_mul_f32_e32 v26, 0x39800000, v26
	v_pk_mul_f32 v[32:33], v[32:33], v[34:35]
	v_pk_fma_f32 v[34:35], v[120:121], v[28:29], v[6:7] op_sel_hi:[1,0,1]
	v_pk_mul_f32 v[32:33], v[32:33], v[36:37]
	v_min_f32_e32 v34, 0x40e00000, v34
	v_min_f32_e32 v35, 0x40e00000, v35
	v_pk_mul_f32 v[36:37], v[34:35], s[76:77] op_sel_hi:[1,0]
	v_pk_fma_f32 v[28:29], v[116:117], v[28:29], v[4:5] op_sel_hi:[1,0,1]
	v_exp_f32_e32 v36, v36
	v_exp_f32_e32 v37, v37
	v_med3_f32 v28, v28, s54, v228
	v_med3_f32 v29, v29, s54, v228
	v_cvt_pk_fp8_f32 v39, v32, v33
	v_pk_add_f32 v[36:37], v[36:37], 1.0 op_sel_hi:[1,0]
	v_pk_fma_f32 v[28:29], v[28:29], 4.0, 4.0 op_sel_hi:[1,0,0]
	v_rcp_f32_e32 v36, v36
	v_rcp_f32_e32 v37, v37
	v_pk_mul_f32 v[2:3], v[34:35], v[28:29]
	v_pk_fma_f32 v[28:29], v[110:111], v[26:27], v[22:23] op_sel_hi:[1,0,1]
	v_cvt_pk_fp8_f32 v38, v30, v31 op_sel:[0,0,1]
	v_pk_mul_f32 v[2:3], v[2:3], v[36:37]
	v_min_f32_e32 v28, 0x40e00000, v28
	v_min_f32_e32 v29, 0x40e00000, v29
	v_cvt_pk_fp8_f32 v39, v2, v3 op_sel:[0,0,1]
	v_add_u32_e32 v2, 0x80, v20
	v_pk_mul_f32 v[30:31], v[28:29], s[76:77] op_sel_hi:[1,0]
	v_ashrrev_i32_e32 v3, 31, v2
	v_exp_f32_e32 v30, v30
	v_exp_f32_e32 v31, v31
	v_lshlrev_b64 v[2:3], 11, v[2:3]
	v_lshl_add_u64 v[2:3], s[66:67], 0, v[2:3]
	v_lshl_add_u64 v[2:3], v[2:3], 0, v[18:19]
	global_store_dwordx2 v[2:3], v[38:39], off
	v_pk_fma_f32 v[2:3], v[106:107], v[26:27], v[16:17] op_sel_hi:[1,0,1]
	v_pk_add_f32 v[30:31], v[30:31], 1.0 op_sel_hi:[1,0]
	v_med3_f32 v2, v2, s54, v228
	v_rcp_f32_e32 v30, v30
	v_rcp_f32_e32 v31, v31
	v_med3_f32 v3, v3, s54, v228
	v_pk_fma_f32 v[2:3], v[2:3], 4.0, 4.0 op_sel_hi:[1,0,0]
	v_mov_b32_e32 v36, v199
	v_pk_mul_f32 v[2:3], v[28:29], v[2:3]
	v_pk_fma_f32 v[28:29], v[112:113], v[26:27], v[14:15] op_sel_hi:[1,0,1]
	v_pk_mul_f32 v[2:3], v[2:3], v[30:31]
	v_min_f32_e32 v28, 0x40e00000, v28
	v_min_f32_e32 v29, 0x40e00000, v29
	v_pk_fma_f32 v[30:31], v[108:109], v[26:27], v[12:13] op_sel_hi:[1,0,1]
	v_pk_mul_f32 v[32:33], v[28:29], s[76:77] op_sel_hi:[1,0]
	v_med3_f32 v30, v30, s54, v228
	v_exp_f32_e32 v32, v32
	v_exp_f32_e32 v33, v33
	v_med3_f32 v31, v31, s54, v228
	v_pk_fma_f32 v[30:31], v[30:31], 4.0, 4.0 op_sel_hi:[1,0,0]
	v_cvt_pk_fp8_f32 v36, v2, v3
	v_pk_mul_f32 v[28:29], v[28:29], v[30:31]
	v_pk_fma_f32 v[30:31], v[102:103], v[26:27], v[10:11] op_sel_hi:[1,0,1]
	v_pk_add_f32 v[32:33], v[32:33], 1.0 op_sel_hi:[1,0]
	v_min_f32_e32 v30, 0x40e00000, v30
	v_min_f32_e32 v31, 0x40e00000, v31
	v_pk_mul_f32 v[34:35], v[30:31], s[76:77] op_sel_hi:[1,0]
	v_rcp_f32_e32 v32, v32
	v_rcp_f32_e32 v33, v33
	v_exp_f32_e32 v34, v34
	v_exp_f32_e32 v35, v35
	v_mov_b32_e32 v37, v199
	v_pk_mul_f32 v[28:29], v[28:29], v[32:33]
	v_pk_fma_f32 v[32:33], v[98:99], v[26:27], v[8:9] op_sel_hi:[1,0,1]
	v_pk_add_f32 v[34:35], v[34:35], 1.0 op_sel_hi:[1,0]
	v_med3_f32 v32, v32, s54, v228
	v_rcp_f32_e32 v34, v34
	v_rcp_f32_e32 v35, v35
	v_med3_f32 v33, v33, s54, v228
	v_pk_fma_f32 v[32:33], v[32:33], 4.0, 4.0 op_sel_hi:[1,0,0]
	v_cvt_pk_fp8_f32 v36, v28, v29 op_sel:[0,0,1]
	v_pk_mul_f32 v[30:31], v[30:31], v[32:33]
	v_pk_fma_f32 v[32:33], v[104:105], v[26:27], v[6:7] op_sel_hi:[1,0,1]
	v_pk_mul_f32 v[30:31], v[30:31], v[34:35]
	v_min_f32_e32 v32, 0x40e00000, v32
	v_min_f32_e32 v33, 0x40e00000, v33
	v_pk_mul_f32 v[34:35], v[32:33], s[76:77] op_sel_hi:[1,0]
	v_pk_fma_f32 v[26:27], v[100:101], v[26:27], v[4:5] op_sel_hi:[1,0,1]
	v_exp_f32_e32 v34, v34
	v_exp_f32_e32 v35, v35
	v_med3_f32 v26, v26, s54, v228
	v_med3_f32 v27, v27, s54, v228
	v_pk_fma_f32 v[26:27], v[26:27], 4.0, 4.0 op_sel_hi:[1,0,0]
	v_pk_add_f32 v[34:35], v[34:35], 1.0 op_sel_hi:[1,0]
	v_cvt_pk_fp8_f32 v37, v30, v31
	v_rcp_f32_e32 v34, v34
	v_rcp_f32_e32 v35, v35
	v_pk_mul_f32 v[2:3], v[32:33], v[26:27]
	v_mul_f32_e32 v26, 0x39800000, v25
	v_pk_fma_f32 v[28:29], v[94:95], v[26:27], v[22:23] op_sel_hi:[1,0,1]
	v_pk_mul_f32 v[2:3], v[2:3], v[34:35]
	v_min_f32_e32 v28, 0x40e00000, v28
	v_min_f32_e32 v29, 0x40e00000, v29
	v_cvt_pk_fp8_f32 v37, v2, v3 op_sel:[0,0,1]
	v_add_u32_e32 v2, 0x90, v20
	v_pk_mul_f32 v[30:31], v[28:29], s[76:77] op_sel_hi:[1,0]
	v_ashrrev_i32_e32 v3, 31, v2
	v_exp_f32_e32 v30, v30
	v_exp_f32_e32 v31, v31
	v_lshlrev_b64 v[2:3], 11, v[2:3]
	v_lshl_add_u64 v[2:3], s[66:67], 0, v[2:3]
	v_lshl_add_u64 v[2:3], v[2:3], 0, v[18:19]
	global_store_dwordx2 v[2:3], v[36:37], off
	v_pk_fma_f32 v[2:3], v[90:91], v[26:27], v[16:17] op_sel_hi:[1,0,1]
	v_pk_add_f32 v[30:31], v[30:31], 1.0 op_sel_hi:[1,0]
	v_med3_f32 v2, v2, s54, v228
	v_rcp_f32_e32 v30, v30
	v_rcp_f32_e32 v31, v31
	v_med3_f32 v3, v3, s54, v228
	v_pk_fma_f32 v[2:3], v[2:3], 4.0, 4.0 op_sel_hi:[1,0,0]
	v_mov_b32_e32 v37, v199
	v_pk_mul_f32 v[2:3], v[28:29], v[2:3]
	v_pk_fma_f32 v[28:29], v[96:97], v[26:27], v[14:15] op_sel_hi:[1,0,1]
	v_pk_mul_f32 v[2:3], v[2:3], v[30:31]
	v_min_f32_e32 v28, 0x40e00000, v28
	v_min_f32_e32 v29, 0x40e00000, v29
	v_pk_fma_f32 v[30:31], v[92:93], v[26:27], v[12:13] op_sel_hi:[1,0,1]
	v_pk_mul_f32 v[32:33], v[28:29], s[76:77] op_sel_hi:[1,0]
	v_med3_f32 v30, v30, s54, v228
	v_exp_f32_e32 v32, v32
	v_exp_f32_e32 v33, v33
	v_med3_f32 v31, v31, s54, v228
	v_pk_fma_f32 v[30:31], v[30:31], 4.0, 4.0 op_sel_hi:[1,0,0]
	v_mov_b32_e32 v36, v199
	v_pk_mul_f32 v[28:29], v[28:29], v[30:31]
	v_pk_fma_f32 v[30:31], v[86:87], v[26:27], v[10:11] op_sel_hi:[1,0,1]
	v_pk_add_f32 v[32:33], v[32:33], 1.0 op_sel_hi:[1,0]
	v_min_f32_e32 v30, 0x40e00000, v30
	v_min_f32_e32 v31, 0x40e00000, v31
	v_pk_mul_f32 v[34:35], v[30:31], s[76:77] op_sel_hi:[1,0]
	v_rcp_f32_e32 v32, v32
	v_rcp_f32_e32 v33, v33
	v_exp_f32_e32 v34, v34
	v_exp_f32_e32 v35, v35
	v_cvt_pk_fp8_f32 v36, v2, v3
	v_pk_mul_f32 v[28:29], v[28:29], v[32:33]
	v_pk_fma_f32 v[32:33], v[82:83], v[26:27], v[8:9] op_sel_hi:[1,0,1]
	v_pk_add_f32 v[34:35], v[34:35], 1.0 op_sel_hi:[1,0]
	v_med3_f32 v32, v32, s54, v228
	v_rcp_f32_e32 v34, v34
	v_rcp_f32_e32 v35, v35
	v_med3_f32 v33, v33, s54, v228
	v_pk_fma_f32 v[32:33], v[32:33], 4.0, 4.0 op_sel_hi:[1,0,0]
	v_mul_f32_e32 v24, 0x39800000, v24
	v_pk_mul_f32 v[30:31], v[30:31], v[32:33]
	v_pk_fma_f32 v[32:33], v[88:89], v[26:27], v[6:7] op_sel_hi:[1,0,1]
	v_pk_mul_f32 v[30:31], v[30:31], v[34:35]
	v_min_f32_e32 v32, 0x40e00000, v32
	v_min_f32_e32 v33, 0x40e00000, v33
	v_pk_mul_f32 v[34:35], v[32:33], s[76:77] op_sel_hi:[1,0]
	v_pk_fma_f32 v[26:27], v[84:85], v[26:27], v[4:5] op_sel_hi:[1,0,1]
	v_exp_f32_e32 v34, v34
	v_exp_f32_e32 v35, v35
	v_med3_f32 v26, v26, s54, v228
	v_med3_f32 v27, v27, s54, v228
	v_cvt_pk_fp8_f32 v37, v30, v31
	v_pk_add_f32 v[34:35], v[34:35], 1.0 op_sel_hi:[1,0]
	v_pk_fma_f32 v[26:27], v[26:27], 4.0, 4.0 op_sel_hi:[1,0,0]
	v_rcp_f32_e32 v34, v34
	v_rcp_f32_e32 v35, v35
	v_pk_mul_f32 v[2:3], v[32:33], v[26:27]
	v_pk_fma_f32 v[22:23], v[78:79], v[24:25], v[22:23] op_sel_hi:[1,0,1]
	v_cvt_pk_fp8_f32 v36, v28, v29 op_sel:[0,0,1]
	v_pk_mul_f32 v[2:3], v[2:3], v[34:35]
	v_min_f32_e32 v22, 0x40e00000, v22
	v_min_f32_e32 v23, 0x40e00000, v23
	v_cvt_pk_fp8_f32 v37, v2, v3 op_sel:[0,0,1]
	v_add_u32_e32 v2, 0xa0, v20
	v_pk_mul_f32 v[26:27], v[22:23], s[76:77] op_sel_hi:[1,0]
	v_ashrrev_i32_e32 v3, 31, v2
	v_exp_f32_e32 v26, v26
	v_exp_f32_e32 v27, v27
	v_lshlrev_b64 v[2:3], 11, v[2:3]
	v_lshl_add_u64 v[2:3], s[66:67], 0, v[2:3]
	v_lshl_add_u64 v[2:3], v[2:3], 0, v[18:19]
	global_store_dwordx2 v[2:3], v[36:37], off
	v_pk_fma_f32 v[2:3], v[74:75], v[24:25], v[16:17] op_sel_hi:[1,0,1]
	v_pk_add_f32 v[16:17], v[26:27], 1.0 op_sel_hi:[1,0]
	v_med3_f32 v2, v2, s54, v228
	v_rcp_f32_e32 v16, v16
	v_rcp_f32_e32 v17, v17
	v_med3_f32 v3, v3, s54, v228
	v_pk_fma_f32 v[12:13], v[76:77], v[24:25], v[12:13] op_sel_hi:[1,0,1]
	v_pk_fma_f32 v[2:3], v[2:3], 4.0, 4.0 op_sel_hi:[1,0,0]
	v_pk_fma_f32 v[14:15], v[80:81], v[24:25], v[14:15] op_sel_hi:[1,0,1]
	v_med3_f32 v12, v12, s54, v228
	v_med3_f32 v13, v13, s54, v228
	v_pk_fma_f32 v[10:11], v[70:71], v[24:25], v[10:11] op_sel_hi:[1,0,1]
	v_pk_mul_f32 v[2:3], v[22:23], v[2:3]
	v_min_f32_e32 v14, 0x40e00000, v14
	v_min_f32_e32 v15, 0x40e00000, v15
	v_pk_fma_f32 v[12:13], v[12:13], 4.0, 4.0 op_sel_hi:[1,0,0]
	v_min_f32_e32 v10, 0x40e00000, v10
	v_min_f32_e32 v11, 0x40e00000, v11
	v_pk_mul_f32 v[2:3], v[2:3], v[16:17]
	v_pk_mul_f32 v[16:17], v[14:15], s[76:77] op_sel_hi:[1,0]
	v_pk_mul_f32 v[12:13], v[14:15], v[12:13]
	v_pk_mul_f32 v[14:15], v[10:11], s[76:77] op_sel_hi:[1,0]
	v_pk_fma_f32 v[8:9], v[66:67], v[24:25], v[8:9] op_sel_hi:[1,0,1]
	v_exp_f32_e32 v14, v14
	v_exp_f32_e32 v15, v15
	v_med3_f32 v8, v8, s54, v228
	v_med3_f32 v9, v9, s54, v228
	v_pk_fma_f32 v[6:7], v[72:73], v[24:25], v[6:7] op_sel_hi:[1,0,1]
	v_pk_fma_f32 v[8:9], v[8:9], 4.0, 4.0 op_sel_hi:[1,0,0]
	v_min_f32_e32 v6, 0x40e00000, v6
	v_min_f32_e32 v7, 0x40e00000, v7
	v_pk_mul_f32 v[8:9], v[10:11], v[8:9]
	v_pk_mul_f32 v[10:11], v[6:7], s[76:77] op_sel_hi:[1,0]
	v_pk_add_f32 v[14:15], v[14:15], 1.0 op_sel_hi:[1,0]
	v_exp_f32_e32 v10, v10
	v_exp_f32_e32 v11, v11
	v_exp_f32_e32 v16, v16
	v_exp_f32_e32 v17, v17
	v_rcp_f32_e32 v14, v14
	v_rcp_f32_e32 v15, v15
	v_pk_add_f32 v[10:11], v[10:11], 1.0 op_sel_hi:[1,0]
	v_pk_add_f32 v[16:17], v[16:17], 1.0 op_sel_hi:[1,0]
	v_pk_fma_f32 v[4:5], v[68:69], v[24:25], v[4:5] op_sel_hi:[1,0,1]
	v_pk_mul_f32 v[8:9], v[8:9], v[14:15]
	v_rcp_f32_e32 v10, v10
	v_rcp_f32_e32 v11, v11
	v_mov_b32_e32 v15, v199
	v_rcp_f32_e32 v16, v16
	v_rcp_f32_e32 v17, v17
	v_med3_f32 v4, v4, s54, v228
	v_med3_f32 v5, v5, s54, v228
	v_mov_b32_e32 v14, v199
	v_cvt_pk_fp8_f32 v15, v8, v9
	v_pk_fma_f32 v[4:5], v[4:5], 4.0, 4.0 op_sel_hi:[1,0,0]
	v_cvt_pk_fp8_f32 v14, v2, v3
	v_pk_mul_f32 v[2:3], v[6:7], v[4:5]
	v_pk_mul_f32 v[12:13], v[12:13], v[16:17]
	v_pk_mul_f32 v[2:3], v[2:3], v[10:11]
	v_cvt_pk_fp8_f32 v14, v12, v13 op_sel:[0,0,1]
	v_cvt_pk_fp8_f32 v15, v2, v3 op_sel:[0,0,1]
	v_add_u32_e32 v2, 0xb0, v20
	v_ashrrev_i32_e32 v3, 31, v2
	v_lshlrev_b64 v[2:3], 11, v[2:3]
	v_lshl_add_u64 v[2:3], s[66:67], 0, v[2:3]
	v_lshl_add_u64 v[2:3], v[2:3], 0, v[18:19]
	global_store_dwordx2 v[2:3], v[14:15], off
	s_cbranch_vccnz .LBB0_719
	s_add_i32 s2, s51, 2
	s_mul_i32 s3, s2, s40
	s_mul_hi_u32 s5, s2, s84
	s_add_i32 s5, s5, s3
	s_mul_i32 s2, s2, s84
	s_add_u32 s2, s2, s87
	s_addc_u32 s3, s5, s38
	v_cmp_ge_i64_e32 vcc, s[2:3], v[196:197]
	v_cmp_lt_i64_e64 s[8:9], s[2:3], v[196:197]
	s_and_b64 vcc, exec, vcc
	s_mov_b32 s29, s4
	s_mov_b32 s30, s39
	s_mov_b32 s31, s6
	s_mov_b32 s34, s41
	s_cbranch_vccz .LBB0_720
	s_andn2_b64 vcc, exec, s[8:9]
	s_cbranch_vccz .LBB0_721

.LBB0_721:
	v_mov_b32_e32 v1, v0
	s_nop 0
	v_ashrrev_i32_e32 v2, 31, v1
	v_lshrrev_b32_e32 v2, 26, v2
	v_lshlrev_b32_e32 v6, 4, v1
	v_add_u32_e32 v2, v1, v2
	v_bfe_i32 v1, v1, 27, 1
	v_lshrrev_b32_e32 v1, 22, v1
	v_add_u32_e32 v1, v6, v1
	v_and_b32_e32 v1, 0xfffffc00, v1
	v_sub_u32_e32 v1, v6, v1
	v_add_u32_e32 v6, 0x2000, v6
	v_ashrrev_i32_e32 v7, 31, v6
	v_lshrrev_b32_e32 v7, 22, v7
	v_add_u32_e32 v7, v6, v7
	v_ashrrev_i32_e32 v10, 6, v2
	v_lshrrev_b32_e32 v2, 4, v1
	v_ashrrev_i32_e32 v12, 10, v7
	v_bitop3_b32 v1, v2, v1, 32 bitop3:0x6c
	v_mul_i32_i24_e32 v7, 0x400, v12
	v_ashrrev_i32_e32 v3, 31, v1
	v_sub_u32_e32 v6, v6, v7
	v_lshrrev_b32_e32 v3, 26, v3
	v_lshrrev_b32_e32 v7, 4, v6
	v_lshlrev_b32_e32 v2, 3, v10
	v_add_u32_e32 v11, v1, v3
	v_bitop3_b32 v13, v7, v6, 32 bitop3:0x6c
	v_and_b32_e32 v2, -16, v2
	v_ashrrev_i32_e32 v3, 6, v11
	v_ashrrev_i32_e32 v7, 31, v13
	v_add3_u32 v2, v2, s34, v3
	v_lshrrev_b32_e32 v7, 26, v7
	v_ashrrev_i32_e32 v3, 31, v2
	v_lshlrev_b32_e32 v6, 3, v12
	v_add_u32_e32 v14, v13, v7
	v_lshl_add_u64 v[4:5], v[2:3], 2, s[10:11]
	v_add_u32_e32 v2, 0x80, v2
	v_and_b32_e32 v6, -16, v6
	v_ashrrev_i32_e32 v7, 6, v14
	v_ashrrev_i32_e32 v3, 31, v2
	v_add3_u32 v6, v6, s34, v7
	v_lshl_add_u64 v[2:3], v[2:3], 2, s[10:11]
	v_ashrrev_i32_e32 v7, 31, v6
	v_lshl_add_u64 v[8:9], v[6:7], 2, s[10:11]
	global_load_dword v4, v[4:5], off
	s_nop 0
	global_load_dword v5, v[2:3], off
	global_load_dword v7, v[8:9], off
	v_add_u32_e32 v2, 0x80, v6
	v_ashrrev_i32_e32 v3, 31, v2
	v_lshl_add_u64 v[2:3], v[2:3], 2, s[10:11]
	global_load_dword v2, v[2:3], off
	v_and_b32_e32 v8, 0xc0, v11
	v_sub_u32_e32 v1, v1, v8
	v_lshlrev_b32_e32 v3, 5, v10
	v_ashrrev_i16_sdwa v1, v229, sext(v1) dst_sel:DWORD dst_unused:UNUSED_PAD src0_sel:DWORD src1_sel:BYTE_0
	v_and_b32_e32 v3, 32, v3
	v_bfe_i32 v1, v1, 0, 16
	v_and_b32_e32 v8, 0xc0, v14
	v_add_lshl_u32 v3, v3, v1, 1
	v_sub_u32_e32 v1, v13, v8
	v_lshlrev_b32_e32 v6, 5, v12
	v_ashrrev_i16_sdwa v1, v229, sext(v1) dst_sel:DWORD dst_unused:UNUSED_PAD src0_sel:DWORD src1_sel:BYTE_0
	v_and_b32_e32 v6, 32, v6
	v_bfe_i32 v1, v1, 0, 16
	v_add_lshl_u32 v6, v6, v1, 1
	s_waitcnt vmcnt(3)
	v_min_u32_e32 v1, 0x3fff, v4
	s_waitcnt vmcnt(2)
	v_min_u32_e32 v4, 0x3fff, v5
	v_lshl_add_u32 v1, v1, 11, v3
	v_lshl_add_u32 v210, v4, 11, v3
	s_waitcnt vmcnt(1)
	v_min_u32_e32 v3, 0x3fff, v7
	v_lshl_add_u32 v195, v3, 11, v6
	s_waitcnt vmcnt(0)
	v_min_u32_e32 v2, 0x3fff, v2
	v_lshl_add_u32 v212, v2, 11, v6
	s_andn2_b64 vcc, exec, s[64:65]
	s_cbranch_vccnz .LBB0_706
